# speedup vs baseline: 1.1609x; 1.0177x over previous
_Z6conv_kILi128ELi64ELi20ELi64ELi4ELi4ELb0EEvPKDF16_S1_PKfS3_PDF16_S4_S1_fS3_S3_S3_S3_:
	v_readfirstlane_b32 s37, v0
	v_bfe_u32 v10, v0, 3, 3
	v_and_b32_e32 v1, 7, v0
	s_and_b32 s36, s2, 3
	s_ashr_i32 s35, s2, 6
	s_lshl_b32 s3, s2, 3
	s_lshr_b32 s42, s37, 6
	s_and_b32 s33, s2, 56
	v_bitop3_b32 v2, v10, v1, 6 bitop3:0x6c
	s_mul_i32 s2, s36, 5
	v_lshlrev_b32_e32 v4, 3, v2
	s_add_i32 s24, s2, s33
	v_lshl_or_b32 v2, s42, 3, v10
	s_mov_b32 s2, 0x28282829
	s_load_dwordx2 s[28:29], s[0:1], 0x0
	s_load_dwordx2 s[4:5], s[0:1], 0x30
	v_mul_hi_u32 v3, v2, s2
	s_and_b32 s34, s3, 32
	v_lshrrev_b32_e32 v3, 3, v3
	s_movk_i32 s8, 0xffcd
	s_add_i32 s24, s24, -9
	v_mul_lo_u32 v5, v3, s8
	v_add_u32_e32 v103, s24, v3
	s_add_i32 s25, s34, -9
	s_movk_i32 s9, 0x264
	v_add3_u32 v5, s25, v2, v5
	v_cmp_gt_u32_e32 vcc, s9, v2
	v_cmp_gt_u32_e64 s[2:3], 64, v103
	s_and_b64 s[2:3], vcc, s[2:3]
	v_cmp_gt_u32_e32 vcc, 64, v5
	v_and_b32_e32 v102, 63, v0
	s_and_b64 s[6:7], s[2:3], vcc
	s_waitcnt lgkmcnt(0)
	v_mov_b64_e32 v[6:7], s[4:5]
	v_lshlrev_b32_e32 v2, 1, v4
	s_and_saveexec_b64 s[2:3], s[6:7]
	s_lshl_b32 s10, s35, 13
	v_lshlrev_b32_e32 v3, 6, v103
	v_or3_b32 v6, v3, s10, v5
	v_ashrrev_i32_e32 v7, 31, v6
	v_lshlrev_b64 v[6:7], 7, v[6:7]
	v_lshl_add_u64 v[6:7], s[28:29], 0, v[6:7]
	v_mov_b32_e32 v3, 0
	v_lshl_add_u64 v[6:7], v[6:7], 0, v[2:3]
	s_or_b64 exec, exec, s[2:3]
	s_lshl_b32 s44, s42, 10
	v_lshlrev_b32_e32 v104, 4, v102
	v_or_b32_e32 v3, s44, v104
	s_add_i32 s11, s42, 8
	v_readfirstlane_b32 s2, v3
	s_mov_b32 m0, s2
	v_lshl_or_b32 v3, s11, 3, v10
	global_load_lds_dwordx4 v[6:7], off
	s_mov_b32 s10, 0x50505051
	v_mul_hi_u32 v6, v3, s10
	v_lshrrev_b32_e32 v6, 4, v6
	v_mul_lo_u32 v7, v6, s8
	v_add_u32_e32 v105, s24, v6
	v_add3_u32 v8, s25, v3, v7
	v_cmp_gt_u32_e32 vcc, s9, v3
	v_cmp_gt_u32_e64 s[2:3], 64, v105
	s_and_b64 s[2:3], vcc, s[2:3]
	v_cmp_gt_u32_e32 vcc, 64, v8
	s_and_b64 s[8:9], s[2:3], vcc
	v_mov_b64_e32 v[6:7], s[4:5]
	s_and_saveexec_b64 s[2:3], s[8:9]
	s_lshl_b32 s12, s35, 13
	v_lshlrev_b32_e32 v3, 6, v105
	v_or3_b32 v6, v3, s12, v8
	v_ashrrev_i32_e32 v7, 31, v6
	v_lshlrev_b64 v[6:7], 7, v[6:7]
	v_lshl_add_u64 v[6:7], s[28:29], 0, v[6:7]
	v_mov_b32_e32 v3, 0
	v_lshl_add_u64 v[6:7], v[6:7], 0, v[2:3]
	s_or_b64 exec, exec, s[2:3]
	s_lshl_b32 s45, s11, 10
	v_or_b32_e32 v3, s45, v104
	s_add_i32 s14, s42, 16
	v_readfirstlane_b32 s2, v3
	s_mov_b32 m0, s2
	v_lshl_or_b32 v3, s14, 3, v10
	global_load_lds_dwordx4 v[6:7], off
	v_mul_hi_u32 v6, v3, s10
	v_lshrrev_b32_e32 v6, 4, v6
	s_movk_i32 s12, 0xffcd
	v_mul_lo_u32 v7, v6, s12
	v_add_u32_e32 v106, s24, v6
	s_movk_i32 s13, 0x264
	v_add3_u32 v9, s25, v3, v7
	v_cmp_gt_u32_e32 vcc, s13, v3
	v_cmp_gt_u32_e64 s[2:3], 64, v106
	s_and_b64 s[2:3], vcc, s[2:3]
	v_cmp_gt_u32_e32 vcc, 64, v9
	s_and_b64 s[10:11], s[2:3], vcc
	v_mov_b64_e32 v[6:7], s[4:5]
	s_and_saveexec_b64 s[2:3], s[10:11]
	s_lshl_b32 s15, s35, 13
	v_lshlrev_b32_e32 v3, 6, v106
	v_or3_b32 v6, v3, s15, v9
	v_ashrrev_i32_e32 v7, 31, v6
	v_lshlrev_b64 v[6:7], 7, v[6:7]
	v_lshl_add_u64 v[6:7], s[28:29], 0, v[6:7]
	v_mov_b32_e32 v3, 0
	v_lshl_add_u64 v[6:7], v[6:7], 0, v[2:3]
	s_or_b64 exec, exec, s[2:3]
	s_lshl_b32 s46, s14, 10
	v_or_b32_e32 v3, s46, v104
	s_add_i32 s15, s42, 24
	v_readfirstlane_b32 s2, v3
	s_mov_b32 m0, s2
	v_lshl_or_b32 v3, s15, 3, v10
	global_load_lds_dwordx4 v[6:7], off
	s_mov_b32 s14, 0x50505051
	v_mul_hi_u32 v6, v3, s14
	v_lshrrev_b32_e32 v6, 4, v6
	v_mul_lo_u32 v7, v6, s12
	v_add_u32_e32 v107, s24, v6
	v_add3_u32 v11, s25, v3, v7
	v_cmp_gt_u32_e32 vcc, s13, v3
	v_cmp_gt_u32_e64 s[2:3], 64, v107
	s_and_b64 s[2:3], vcc, s[2:3]
	v_cmp_gt_u32_e32 vcc, 64, v11
	s_and_b64 s[12:13], s[2:3], vcc
	v_mov_b64_e32 v[6:7], s[4:5]
	s_and_saveexec_b64 s[2:3], s[12:13]
	s_lshl_b32 s16, s35, 13
	v_lshlrev_b32_e32 v3, 6, v107
	v_or3_b32 v6, v3, s16, v11
	v_ashrrev_i32_e32 v7, 31, v6
	v_lshlrev_b64 v[6:7], 7, v[6:7]
	v_lshl_add_u64 v[6:7], s[28:29], 0, v[6:7]
	v_mov_b32_e32 v3, 0
	v_lshl_add_u64 v[6:7], v[6:7], 0, v[2:3]
	s_or_b64 exec, exec, s[2:3]
	s_lshl_b32 s47, s15, 10
	v_or_b32_e32 v3, s47, v104
	s_add_i32 s18, s42, 32
	v_readfirstlane_b32 s2, v3
	s_mov_b32 m0, s2
	v_lshl_or_b32 v3, s18, 3, v10
	global_load_lds_dwordx4 v[6:7], off
	v_mul_hi_u32 v6, v3, s14
	v_lshrrev_b32_e32 v6, 4, v6
	s_movk_i32 s16, 0xffcd
	v_mul_lo_u32 v7, v6, s16
	v_add_u32_e32 v108, s24, v6
	s_movk_i32 s17, 0x264
	v_add3_u32 v12, s25, v3, v7
	v_cmp_gt_u32_e32 vcc, s17, v3
	v_cmp_gt_u32_e64 s[2:3], 64, v108
	s_and_b64 s[2:3], vcc, s[2:3]
	v_cmp_gt_u32_e32 vcc, 64, v12
	s_and_b64 s[14:15], s[2:3], vcc
	v_mov_b64_e32 v[6:7], s[4:5]
	s_and_saveexec_b64 s[2:3], s[14:15]
	s_lshl_b32 s19, s35, 13
	v_lshlrev_b32_e32 v3, 6, v108
	v_or3_b32 v6, v3, s19, v12
	v_ashrrev_i32_e32 v7, 31, v6
	v_lshlrev_b64 v[6:7], 7, v[6:7]
	v_lshl_add_u64 v[6:7], s[28:29], 0, v[6:7]
	v_mov_b32_e32 v3, 0
	v_lshl_add_u64 v[6:7], v[6:7], 0, v[2:3]
	s_or_b64 exec, exec, s[2:3]
	s_lshl_b32 s48, s18, 10
	v_or_b32_e32 v3, s48, v104
	s_add_i32 s19, s42, 40
	v_readfirstlane_b32 s2, v3
	s_mov_b32 m0, s2
	v_lshl_or_b32 v3, s19, 3, v10
	global_load_lds_dwordx4 v[6:7], off
	s_mov_b32 s18, 0x50505051
	v_mul_hi_u32 v6, v3, s18
	v_lshrrev_b32_e32 v6, 4, v6
	v_mul_lo_u32 v7, v6, s16
	v_add_u32_e32 v109, s24, v6
	v_add3_u32 v13, s25, v3, v7
	v_cmp_gt_u32_e32 vcc, s17, v3
	v_cmp_gt_u32_e64 s[2:3], 64, v109
	s_and_b64 s[2:3], vcc, s[2:3]
	v_cmp_gt_u32_e32 vcc, 64, v13
	s_and_b64 s[16:17], s[2:3], vcc
	v_mov_b64_e32 v[6:7], s[4:5]
	s_and_saveexec_b64 s[2:3], s[16:17]
	s_lshl_b32 s20, s35, 13
	v_lshlrev_b32_e32 v3, 6, v109
	v_or3_b32 v6, v3, s20, v13
	v_ashrrev_i32_e32 v7, 31, v6
	v_lshlrev_b64 v[6:7], 7, v[6:7]
	v_lshl_add_u64 v[6:7], s[28:29], 0, v[6:7]
	v_mov_b32_e32 v3, 0
	v_lshl_add_u64 v[6:7], v[6:7], 0, v[2:3]
	s_or_b64 exec, exec, s[2:3]
	s_lshl_b32 s49, s19, 10
	v_or_b32_e32 v3, s49, v104
	s_add_i32 s22, s42, 48
	v_readfirstlane_b32 s2, v3
	s_mov_b32 m0, s2
	v_lshl_or_b32 v3, s22, 3, v10
	global_load_lds_dwordx4 v[6:7], off
	v_mul_hi_u32 v6, v3, s18
	v_lshrrev_b32_e32 v6, 4, v6
	s_movk_i32 s20, 0xffcd
	v_mul_lo_u32 v7, v6, s20
	v_add_u32_e32 v110, s24, v6
	s_movk_i32 s21, 0x264
	v_add3_u32 v14, s25, v3, v7
	v_cmp_gt_u32_e32 vcc, s21, v3
	v_cmp_gt_u32_e64 s[2:3], 64, v110
	s_and_b64 s[2:3], vcc, s[2:3]
	v_cmp_gt_u32_e32 vcc, 64, v14
	s_and_b64 s[18:19], s[2:3], vcc
	v_mov_b64_e32 v[6:7], s[4:5]
	s_and_saveexec_b64 s[2:3], s[18:19]
	s_lshl_b32 s23, s35, 13
	v_lshlrev_b32_e32 v3, 6, v110
	v_or3_b32 v6, v3, s23, v14
	v_ashrrev_i32_e32 v7, 31, v6
	v_lshlrev_b64 v[6:7], 7, v[6:7]
	v_lshl_add_u64 v[6:7], s[28:29], 0, v[6:7]
	v_mov_b32_e32 v3, 0
	v_lshl_add_u64 v[6:7], v[6:7], 0, v[2:3]
	s_or_b64 exec, exec, s[2:3]
	s_lshl_b32 s50, s22, 10
	v_or_b32_e32 v3, s50, v104
	s_add_i32 s23, s42, 56
	v_readfirstlane_b32 s2, v3
	s_mov_b32 m0, s2
	v_lshl_or_b32 v3, s23, 3, v10
	global_load_lds_dwordx4 v[6:7], off
	s_mov_b32 s22, 0x50505051
	v_mul_hi_u32 v6, v3, s22
	v_lshrrev_b32_e32 v6, 4, v6
	v_mul_lo_u32 v7, v6, s20
	v_add_u32_e32 v113, s24, v6
	v_add3_u32 v15, s25, v3, v7
	v_cmp_gt_u32_e32 vcc, s21, v3
	v_cmp_gt_u32_e64 s[2:3], 64, v113
	s_and_b64 s[2:3], vcc, s[2:3]
	v_cmp_gt_u32_e32 vcc, 64, v15
	s_and_b64 s[20:21], s[2:3], vcc
	v_mov_b64_e32 v[6:7], s[4:5]
	s_and_saveexec_b64 s[2:3], s[20:21]
	s_lshl_b32 s26, s35, 13
	v_lshlrev_b32_e32 v3, 6, v113
	v_or3_b32 v6, v3, s26, v15
	v_ashrrev_i32_e32 v7, 31, v6
	v_lshlrev_b64 v[6:7], 7, v[6:7]
	v_lshl_add_u64 v[6:7], s[28:29], 0, v[6:7]
	v_mov_b32_e32 v3, 0
	v_lshl_add_u64 v[6:7], v[6:7], 0, v[2:3]
	s_or_b64 exec, exec, s[2:3]
	s_lshl_b32 s51, s23, 10
	v_or_b32_e32 v3, s51, v104
	s_add_i32 s26, s42, 64
	v_readfirstlane_b32 s2, v3
	s_mov_b32 m0, s2
	v_lshl_or_b32 v3, s26, 3, v10
	global_load_lds_dwordx4 v[6:7], off
	v_mul_hi_u32 v6, v3, s22
	v_lshrrev_b32_e32 v6, 4, v6
	s_movk_i32 s2, 0xffcd
	v_mul_lo_u32 v7, v6, s2
	v_add_u32_e32 v114, s24, v6
	s_movk_i32 s2, 0x264
	v_add3_u32 v16, s25, v3, v7
	v_cmp_gt_u32_e32 vcc, s2, v3
	v_cmp_gt_u32_e64 s[2:3], 64, v114
	s_and_b64 s[2:3], vcc, s[2:3]
	v_cmp_gt_u32_e32 vcc, 64, v16
	s_and_b64 s[22:23], s[2:3], vcc
	s_xor_b64 s[2:3], s[22:23], -1
	s_and_saveexec_b64 s[30:31], s[2:3]
	s_xor_b64 s[2:3], exec, s[30:31]
	s_lshl_b32 s27, s35, 13
	s_or_saveexec_b64 s[2:3], s[2:3]
	v_mov_b32_e32 v17, s27
	v_mov_b64_e32 v[6:7], s[4:5]
	s_xor_b64 exec, exec, s[2:3]
	s_lshl_b32 s27, s35, 13
	v_lshlrev_b32_e32 v3, 6, v114
	v_or3_b32 v6, v3, s27, v16
	v_ashrrev_i32_e32 v7, 31, v6
	v_lshlrev_b64 v[6:7], 7, v[6:7]
	v_lshl_add_u64 v[6:7], s[28:29], 0, v[6:7]
	v_mov_b32_e32 v3, 0
	v_lshl_add_u64 v[6:7], v[6:7], 0, v[2:3]
	v_mov_b32_e32 v17, s27
	s_or_b64 exec, exec, s[2:3]
	s_lshl_b32 s38, s26, 10
	v_or_b32_e32 v2, s38, v104
	s_add_i32 s41, s42, 0x48
	v_readfirstlane_b32 s2, v2
	s_mov_b32 m0, s2
	v_lshl_or_b32 v2, s41, 3, v10
	global_load_lds_dwordx4 v[6:7], off
	s_mov_b32 s2, 0x50505051
	v_mul_hi_u32 v3, v2, s2
	v_lshrrev_b32_e32 v3, 4, v3
	s_movk_i32 s2, 0xffcd
	s_load_dwordx2 s[30:31], s[0:1], 0x8
	v_mul_lo_u32 v6, v3, s2
	v_add_u32_e32 v115, s24, v3
	s_movk_i32 s2, 0x264
	v_add3_u32 v6, s25, v2, v6
	v_cmp_gt_u32_e32 vcc, s2, v2
	v_cmp_gt_u32_e64 s[2:3], 64, v115
	s_and_b64 s[2:3], vcc, s[2:3]
	v_cmp_gt_u32_e32 vcc, 64, v6
	s_and_b64 s[24:25], s[2:3], vcc
	s_xor_b64 s[2:3], s[24:25], -1
	s_and_saveexec_b64 s[26:27], s[2:3]
	s_xor_b64 s[2:3], exec, s[26:27]
	s_or_saveexec_b64 s[26:27], s[2:3]
	s_load_dwordx2 s[2:3], s[0:1], 0x28
	v_mov_b64_e32 v[2:3], s[4:5]
	s_xor_b64 exec, exec, s[26:27]
	v_lshlrev_b32_e32 v2, 6, v115
	v_or3_b32 v2, v2, v17, v6
	v_ashrrev_i32_e32 v3, 31, v2
	v_lshlrev_b64 v[2:3], 7, v[2:3]
	v_lshl_add_u64 v[2:3], s[28:29], 0, v[2:3]
	v_lshlrev_b32_e32 v18, 1, v4
	v_mov_b32_e32 v19, 0
	v_lshl_add_u64 v[2:3], v[2:3], 0, v[18:19]
	s_or_b64 exec, exec, s[26:27]
	v_lshrrev_b32_e32 v112, 4, v102
	v_lshl_or_b32 v7, v10, 6, s44
	v_bitop3_b32 v10, v112, v0, 6 bitop3:0x78
	v_and_b32_e32 v111, 15, v0
	v_lshlrev_b32_e32 v10, 4, v10
	s_lshr_b32 s40, s37, 8
	v_lshl_or_b32 v10, v111, 7, v10
	v_lshl_or_b32 v10, s40, 13, v10
	s_lshl_b32 s41, s41, 10
	s_movk_i32 s26, 0xdc0
	v_add_u32_e32 v118, 0x14000, v10
	v_or_b32_e32 v10, s41, v104
	v_and_or_b32 v7, v7, s26, v4
	v_readfirstlane_b32 s26, v10
	s_mov_b32 m0, s26
	s_lshl_b32 s55, s42, 11
	s_mul_hi_u32 s26, s37, 0x51eb851f
	s_and_b32 s39, s42, 3
	s_add_i32 s42, s55, 0x14000
	s_lshr_b32 s27, s26, 13
	s_lshr_b32 s52, s26, 14
	s_bitcmp1_b32 s26, 13
	s_cselect_b32 s26, 0x190, 0
	s_sub_i32 s27, s36, s27
	s_add_i32 s27, s27, s52
	s_mulk_i32 s27, 0x64
	s_add_i32 s26, s26, s40
	s_add_i32 s26, s26, s27
	s_ashr_i32 s27, s26, 31
	s_lshl_b64 s[26:27], s[26:27], 13
	s_waitcnt lgkmcnt(0)
	s_add_u32 s26, s30, s26
	s_addc_u32 s27, s31, s27
	s_add_i32 s52, s40, 20
	global_load_lds_dwordx4 v[2:3], off
	v_lshlrev_b32_e32 v2, 1, v7
	s_mov_b32 m0, s42
	s_mul_hi_u32 s53, s52, 0x28f5c29
	global_load_lds_dwordx4 v2, s[26:27]
	s_add_i32 m0, s55, 0x14400
	s_lshr_b32 s56, s53, 1
	s_bitcmp1_b32 s53, 0
	s_cselect_b32 s57, 0x190, 0
	s_sub_i32 s53, s36, s53
	s_add_i32 s53, s53, s56
	s_mulk_i32 s53, 0x64
	s_add_i32 s52, s57, s52
	s_add_i32 s52, s52, s53
	v_mov_b32_e32 v3, 0
	s_ashr_i32 s53, s52, 31
	v_lshl_add_u64 v[18:19], s[26:27], 0, v[2:3]
	s_mov_b64 s[26:27], 0x400
	s_lshl_b64 s[52:53], s[52:53], 13
	v_lshl_add_u64 v[18:19], v[18:19], 0, s[26:27]
	s_add_u32 s52, s30, s52
	global_load_lds_dwordx4 v[18:19], off
	s_addc_u32 s53, s31, s53
	s_add_i32 m0, s55, 0x18000
	v_lshl_add_u64 v[18:19], s[52:53], 0, v[2:3]
	global_load_lds_dwordx4 v2, s[52:53]
	s_add_i32 s52, s40, 40
	s_mul_hi_u32 s53, s52, 0x28f5c29
	s_add_i32 m0, s55, 0x18400
	s_lshr_b32 s56, s53, 1
	s_bitcmp1_b32 s53, 0
	s_cselect_b32 s57, 0x190, 0
	s_sub_i32 s53, s36, s53
	s_add_i32 s53, s53, s56
	s_mulk_i32 s53, 0x64
	s_add_i32 s52, s57, s52
	s_add_i32 s52, s52, s53
	s_ashr_i32 s53, s52, 31
	s_lshl_b64 s[52:53], s[52:53], 13
	s_add_u32 s52, s30, s52
	v_lshl_add_u64 v[18:19], v[18:19], 0, s[26:27]
	s_addc_u32 s53, s31, s53
	global_load_lds_dwordx4 v[18:19], off
	s_add_i32 m0, s55, 0x1c000
	v_lshl_add_u64 v[18:19], s[52:53], 0, v[2:3]
	global_load_lds_dwordx4 v2, s[52:53]
	v_lshl_add_u64 v[18:19], v[18:19], 0, s[26:27]
	s_add_i32 m0, s55, 0x1c400
	s_mul_hi_u32 s52, s40, 0x28f5c29
	global_load_lds_dwordx4 v[18:19], off
	s_mulk_i32 s52, 0x64
	s_sub_i32 s52, s40, s52
	s_mul_i32 s53, s52, 0x67
	s_bfe_u32 s53, s53, 0x5000b
	s_mul_i32 s53, s53, 31
	s_mul_i32 s54, s39, 0x66
	s_and_b32 s53, s53, 0xff
	v_add_u32_e32 v116, s54, v111
	s_add_i32 s52, s52, s53
	s_waitcnt vmcnt(4) lgkmcnt(0)
	s_barrier
	ds_read_b128 v[66:69], v118
	v_add_u32_e32 v7, s52, v116
	v_add_u32_e32 v117, 51, v116
	ds_read_b128 v[70:73], v118 offset:2048
	v_lshlrev_b32_e32 v10, 7, v7
	v_bitop3_b32 v7, v7, v112, 6 bitop3:0x6c
	v_lshl_or_b32 v139, v7, 4, v10
	ds_read_b128 v[74:77], v139
	v_add_u32_e32 v7, s52, v117
	ds_read_b128 v[78:81], v139 offset:2048
	v_lshlrev_b32_e32 v10, 7, v7
	v_bitop3_b32 v7, v7, v112, 6 bitop3:0x6c
	v_lshl_or_b32 v140, v7, 4, v10
	ds_read_b128 v[86:89], v140
	ds_read_b128 v[82:85], v140 offset:2048
	ds_read_b128 v[94:97], v118 offset:4096
	ds_read_b128 v[90:93], v118 offset:6144
	v_add_u32_e32 v120, v17, v5
	v_lshlrev_b32_e32 v4, 1, v4
	v_mov_b32_e32 v5, v3
	v_lshl_add_u64 v[98:99], s[28:29], 0, v[4:5]
	s_add_i32 s28, s40, s54
	v_xor_b32_e32 v119, 64, v118
	s_mov_b32 s43, 0
	v_add_u32_e32 v121, v17, v8
	v_add_u32_e32 v122, v17, v9
	v_add_u32_e32 v123, v17, v11
	v_add_u32_e32 v124, v17, v12
	v_add_u32_e32 v125, v17, v13
	v_add_u32_e32 v126, v17, v14
	v_add_u32_e32 v127, v17, v15
	v_add_u32_e32 v128, v17, v16
	v_add_u32_e32 v129, v17, v6
	v_lshl_add_u64 v[100:101], s[30:31], 0, v[2:3]
	v_add_u32_e32 v130, s28, v111
	v_add_u32_e32 v131, s44, v104
	v_add_u32_e32 v132, s45, v104
	v_add_u32_e32 v133, s46, v104
	v_add_u32_e32 v134, s47, v104
	v_add_u32_e32 v135, s48, v104
	v_add_u32_e32 v136, s49, v104
	v_add_u32_e32 v137, s50, v104
	v_add_u32_e32 v138, s51, v104
	s_mov_b32 s30, s40
	s_mov_b32 s31, s40
	s_mov_b32 s44, 0
	s_mov_b32 s45, 0
	v_mov_b32_e32 v2, v3
	v_mov_b32_e32 v4, v3
	v_mov_b32_e32 v6, v3
	v_mov_b32_e32 v7, v3
	v_mov_b32_e32 v8, v3
	v_mov_b32_e32 v9, v3
	v_mov_b32_e32 v14, v3
	v_mov_b32_e32 v15, v3
	v_mov_b32_e32 v16, v3
	v_mov_b32_e32 v17, v3
	v_mov_b32_e32 v30, v3
	v_mov_b32_e32 v31, v3
	v_mov_b32_e32 v32, v3
	v_mov_b32_e32 v33, v3
	v_mov_b32_e32 v34, v3
	v_mov_b32_e32 v35, v3
	v_mov_b32_e32 v36, v3
	v_mov_b32_e32 v37, v3
	v_mov_b32_e32 v38, v3
	v_mov_b32_e32 v39, v3
	v_mov_b32_e32 v40, v3
	v_mov_b32_e32 v41, v3
	v_mov_b32_e32 v42, v3
	v_mov_b32_e32 v43, v3
	v_mov_b32_e32 v44, v3
	v_mov_b32_e32 v45, v3
	v_mov_b32_e32 v46, v3
	v_mov_b32_e32 v47, v3
	v_mov_b32_e32 v48, v3
	v_mov_b32_e32 v49, v3
	v_mov_b32_e32 v50, v3
	v_mov_b32_e32 v51, v3
	v_mov_b32_e32 v52, v3
	v_mov_b32_e32 v53, v3
	v_mov_b32_e32 v54, v3
	v_mov_b32_e32 v55, v3
	v_mov_b32_e32 v56, v3
	v_mov_b32_e32 v57, v3
	v_mov_b32_e32 v58, v3
	v_mov_b32_e32 v59, v3
	v_mov_b32_e32 v60, v3
	v_mov_b32_e32 v61, v3
	v_mov_b32_e32 v62, v3
	v_mov_b32_e32 v63, v3
	v_mov_b32_e32 v64, v3
	v_mov_b32_e32 v65, v3
	v_mov_b32_e32 v26, v3
	v_mov_b32_e32 v27, v3
	v_mov_b32_e32 v28, v3
	v_mov_b32_e32 v29, v3
	v_mov_b32_e32 v18, v3
	v_mov_b32_e32 v19, v3
	v_mov_b32_e32 v20, v3
	v_mov_b32_e32 v21, v3
	v_mov_b32_e32 v22, v3
	v_mov_b32_e32 v23, v3
	v_mov_b32_e32 v24, v3
	v_mov_b32_e32 v25, v3
	v_mov_b32_e32 v10, v3
	v_mov_b32_e32 v11, v3
	v_mov_b32_e32 v12, v3
	v_mov_b32_e32 v13, v3
	s_mov_b32 s60, 0
	s_mov_b32 s61, 5
	s_mov_b32 s62, 0
	s_mov_b32 s65, 0
	s_mov_b32 s66, 0
	s_mul_i32 s73, s36, 0x64
	s_add_i32 s73, s73, s40
	s_mov_b32 s68, s73
	s_mov_b32 s74, s40
	v_mov_b32_e32 v183, v119
	s_waitcnt lgkmcnt(0)
.Lc6_loop:
	s_waitcnt vmcnt(2)
	s_barrier
	s_waitcnt lgkmcnt(3)
	v_mfma_f32_16x16x32_f16 v[62:65], v[66:69], v[74:77], v[62:65]
	ds_read_b128 v[142:145], v183
	v_mfma_f32_16x16x32_f16 v[58:61], v[70:73], v[74:77], v[58:61]
	v_xor_b32_e32 v180, 64, v140
	s_add_i32 s67, s62, 60
	s_add_i32 s67, s67, s68
	s_lshl_b32 s64, s67, 13
	s_waitcnt lgkmcnt(3)
	v_mfma_f32_16x16x32_f16 v[46:49], v[66:69], v[78:81], v[46:49]
	ds_read_b128 v[146:149], v183 offset:2048
	v_lshl_add_u64 v[174:175], v[100:101], 0, s[64:65]
	s_add_i32 s69, s43, 0xc000
	s_and_b32 s69, s69, 0xc000
	s_add_i32 s69, s69, s42
	v_mfma_f32_16x16x32_f16 v[42:45], v[70:73], v[78:81], v[42:45]
	v_xor_b32_e32 v181, 64, v139
	s_mov_b32 m0, s69
	s_add_i32 s70, s43, 0x4000
	global_load_lds_dwordx4 v[174:175], off
	v_mfma_f32_16x16x32_f16 v[30:33], v[66:69], v[86:89], v[30:33]
	ds_read_b128 v[158:161], v180
	v_mfma_f32_16x16x32_f16 v[14:17], v[70:73], v[86:89], v[14:17]
	s_and_b32 s70, s70, 0xc000
	s_add_i32 s71, s69, 0x400
	v_lshl_add_u64 v[176:177], v[174:175], 0, s[26:27]
	v_mfma_f32_16x16x32_f16 v[26:29], v[66:69], v[82:85], v[26:29]
	ds_read_b128 v[162:165], v180 offset:2048
	v_mfma_f32_16x16x32_f16 v[18:21], v[70:73], v[82:85], v[18:21]
	v_add_u32_e32 v182, s70, v118
	s_add_i32 s72, s74, 102
	s_waitcnt lgkmcnt(5)
	v_mfma_f32_16x16x32_f16 v[54:57], v[94:97], v[74:77], v[54:57]
	ds_read_b128 v[150:153], v181
	s_waitcnt lgkmcnt(5)
	v_mfma_f32_16x16x32_f16 v[50:53], v[90:93], v[74:77], v[50:53]
	v_mfma_f32_16x16x32_f16 v[38:41], v[94:97], v[78:81], v[38:41]
	ds_read_b128 v[154:157], v181 offset:2048
	v_mfma_f32_16x16x32_f16 v[34:37], v[90:93], v[78:81], v[34:37]
	v_add_u32_e32 v178, s72, v116
	v_mfma_f32_16x16x32_f16 v[6:9], v[94:97], v[86:89], v[6:9]
	ds_read_b128 v[166:169], v183 offset:4096
	v_mfma_f32_16x16x32_f16 v[2:5], v[90:93], v[86:89], v[2:5]
	v_lshlrev_b32_e32 v179, 7, v178
	v_bitop3_b32 v178, v178, v112, 6 bitop3:0x6c
	v_mfma_f32_16x16x32_f16 v[22:25], v[94:97], v[82:85], v[22:25]
	ds_read_b128 v[170:173], v183 offset:6144
	v_mfma_f32_16x16x32_f16 v[10:13], v[90:93], v[82:85], v[10:13]
	v_lshl_or_b32 v140, v178, 4, v179
	v_add_u32_e32 v183, s70, v119
	s_waitcnt lgkmcnt(3)
	v_mfma_f32_16x16x32_f16 v[62:65], v[142:145], v[150:153], v[62:65]
	ds_read_b128 v[66:69], v182
	v_mfma_f32_16x16x32_f16 v[58:61], v[146:149], v[150:153], v[58:61]
	s_mov_b32 m0, s71
	s_addk_i32 s43, 0x4000
	global_load_lds_dwordx4 v[176:177], off
	s_waitcnt lgkmcnt(3)
	v_mfma_f32_16x16x32_f16 v[46:49], v[142:145], v[154:157], v[46:49]
	ds_read_b128 v[70:73], v182 offset:2048
	v_mfma_f32_16x16x32_f16 v[42:45], v[146:149], v[154:157], v[42:45]
	v_mfma_f32_16x16x32_f16 v[30:33], v[142:145], v[158:161], v[30:33]
	ds_read_b128 v[74:77], v140
	v_mfma_f32_16x16x32_f16 v[14:17], v[146:149], v[158:161], v[14:17]
	v_mfma_f32_16x16x32_f16 v[26:29], v[142:145], v[162:165], v[26:29]
	ds_read_b128 v[78:81], v140 offset:2048
	v_mfma_f32_16x16x32_f16 v[18:21], v[146:149], v[162:165], v[18:21]
	s_waitcnt lgkmcnt(5)
	v_mfma_f32_16x16x32_f16 v[54:57], v[166:169], v[150:153], v[54:57]
	s_waitcnt lgkmcnt(4)
	v_mfma_f32_16x16x32_f16 v[50:53], v[170:173], v[150:153], v[50:53]
	v_mfma_f32_16x16x32_f16 v[38:41], v[166:169], v[154:157], v[38:41]
	v_mfma_f32_16x16x32_f16 v[34:37], v[170:173], v[154:157], v[34:37]
	v_mfma_f32_16x16x32_f16 v[6:9], v[166:169], v[158:161], v[6:9]
	ds_read_b128 v[94:97], v182 offset:4096
	v_mfma_f32_16x16x32_f16 v[2:5], v[170:173], v[158:161], v[2:5]
	v_mfma_f32_16x16x32_f16 v[22:25], v[166:169], v[162:165], v[22:25]
	ds_read_b128 v[90:93], v182 offset:6144
	v_mfma_f32_16x16x32_f16 v[10:13], v[170:173], v[162:165], v[10:13]
	s_waitcnt vmcnt(2)
	s_barrier
	s_waitcnt lgkmcnt(5)
	v_mfma_f32_16x16x32_f16 v[62:65], v[66:69], v[86:89], v[62:65]
	ds_read_b128 v[142:145], v183
	s_waitcnt lgkmcnt(5)
	v_mfma_f32_16x16x32_f16 v[58:61], v[70:73], v[86:89], v[58:61]
	v_xor_b32_e32 v180, 64, v140
	s_add_i32 s67, s62, 80
	s_add_i32 s67, s67, s68
	s_lshl_b32 s64, s67, 13
	v_mfma_f32_16x16x32_f16 v[46:49], v[66:69], v[82:85], v[46:49]
	ds_read_b128 v[146:149], v183 offset:2048
	v_lshl_add_u64 v[174:175], v[100:101], 0, s[64:65]
	s_add_i32 s69, s43, 0xc000
	s_and_b32 s69, s69, 0xc000
	s_add_i32 s69, s69, s42
	v_mfma_f32_16x16x32_f16 v[42:45], v[70:73], v[82:85], v[42:45]
	s_mov_b32 m0, s69
	s_add_i32 s70, s43, 0x4000
	global_load_lds_dwordx4 v[174:175], off
	s_waitcnt lgkmcnt(5)
	v_mfma_f32_16x16x32_f16 v[30:33], v[66:69], v[74:77], v[30:33]
	ds_read_b128 v[150:153], v180
	v_mfma_f32_16x16x32_f16 v[14:17], v[70:73], v[74:77], v[14:17]
	s_and_b32 s70, s70, 0xc000
	s_add_i32 s71, s69, 0x400
	v_lshl_add_u64 v[176:177], v[174:175], 0, s[26:27]
	s_waitcnt lgkmcnt(5)
	v_mfma_f32_16x16x32_f16 v[26:29], v[66:69], v[78:81], v[26:29]
	ds_read_b128 v[154:157], v180 offset:2048
	v_mfma_f32_16x16x32_f16 v[18:21], v[70:73], v[78:81], v[18:21]
	v_add_u32_e32 v182, s70, v118
	s_add_i32 s72, s74, 153
	s_waitcnt lgkmcnt(5)
	v_mfma_f32_16x16x32_f16 v[54:57], v[94:97], v[86:89], v[54:57]
	s_waitcnt lgkmcnt(4)
	v_mfma_f32_16x16x32_f16 v[50:53], v[90:93], v[86:89], v[50:53]
	v_mfma_f32_16x16x32_f16 v[38:41], v[94:97], v[82:85], v[38:41]
	v_mfma_f32_16x16x32_f16 v[34:37], v[90:93], v[82:85], v[34:37]
	v_add_u32_e32 v178, s72, v116
	v_mfma_f32_16x16x32_f16 v[6:9], v[94:97], v[74:77], v[6:9]
	ds_read_b128 v[166:169], v183 offset:4096
	v_mfma_f32_16x16x32_f16 v[2:5], v[90:93], v[74:77], v[2:5]
	v_lshlrev_b32_e32 v179, 7, v178
	v_bitop3_b32 v178, v178, v112, 6 bitop3:0x6c
	v_mfma_f32_16x16x32_f16 v[22:25], v[94:97], v[78:81], v[22:25]
	ds_read_b128 v[170:173], v183 offset:6144
	v_mfma_f32_16x16x32_f16 v[10:13], v[90:93], v[78:81], v[10:13]
	v_lshl_or_b32 v140, v178, 4, v179
	v_add_u32_e32 v183, s70, v119
	s_waitcnt lgkmcnt(5)
	v_mfma_f32_16x16x32_f16 v[62:65], v[142:145], v[158:161], v[62:65]
	ds_read_b128 v[66:69], v182
	s_waitcnt lgkmcnt(5)
	v_mfma_f32_16x16x32_f16 v[58:61], v[146:149], v[158:161], v[58:61]
	s_mov_b32 m0, s71
	s_addk_i32 s43, 0x4000
	global_load_lds_dwordx4 v[176:177], off
	v_mfma_f32_16x16x32_f16 v[46:49], v[142:145], v[162:165], v[46:49]
	ds_read_b128 v[70:73], v182 offset:2048
	v_mfma_f32_16x16x32_f16 v[42:45], v[146:149], v[162:165], v[42:45]
	s_waitcnt lgkmcnt(5)
	v_mfma_f32_16x16x32_f16 v[30:33], v[142:145], v[150:153], v[30:33]
	ds_read_b128 v[86:89], v140
	v_mfma_f32_16x16x32_f16 v[14:17], v[146:149], v[150:153], v[14:17]
	s_waitcnt lgkmcnt(5)
	v_mfma_f32_16x16x32_f16 v[26:29], v[142:145], v[154:157], v[26:29]
	ds_read_b128 v[82:85], v140 offset:2048
	v_mfma_f32_16x16x32_f16 v[18:21], v[146:149], v[154:157], v[18:21]
	s_waitcnt lgkmcnt(5)
	v_mfma_f32_16x16x32_f16 v[54:57], v[166:169], v[158:161], v[54:57]
	s_waitcnt lgkmcnt(4)
	v_mfma_f32_16x16x32_f16 v[50:53], v[170:173], v[158:161], v[50:53]
	v_mfma_f32_16x16x32_f16 v[38:41], v[166:169], v[162:165], v[38:41]
	v_mfma_f32_16x16x32_f16 v[34:37], v[170:173], v[162:165], v[34:37]
	v_mfma_f32_16x16x32_f16 v[6:9], v[166:169], v[150:153], v[6:9]
	ds_read_b128 v[94:97], v182 offset:4096
	v_mfma_f32_16x16x32_f16 v[2:5], v[170:173], v[150:153], v[2:5]
	v_mfma_f32_16x16x32_f16 v[22:25], v[166:169], v[154:157], v[22:25]
	ds_read_b128 v[90:93], v182 offset:6144
	v_mfma_f32_16x16x32_f16 v[10:13], v[170:173], v[154:157], v[10:13]
	s_waitcnt vmcnt(2)
	s_barrier
	s_waitcnt lgkmcnt(5)
	v_mfma_f32_16x16x32_f16 v[62:65], v[66:69], v[74:77], v[62:65]
	ds_read_b128 v[142:145], v183
	s_waitcnt lgkmcnt(5)
	v_mfma_f32_16x16x32_f16 v[58:61], v[70:73], v[74:77], v[58:61]
	v_xor_b32_e32 v180, 64, v140
	s_add_i32 s67, s62, 2
	s_add_i32 s67, s67, s68
	s_lshl_b32 s64, s67, 13
	v_mfma_f32_16x16x32_f16 v[46:49], v[66:69], v[78:81], v[46:49]
	ds_read_b128 v[146:149], v183 offset:2048
	v_lshl_add_u64 v[174:175], v[100:101], 0, s[64:65]
	s_add_i32 s69, s43, 0xc000
	s_and_b32 s69, s69, 0xc000
	s_add_i32 s69, s69, s42
	v_mfma_f32_16x16x32_f16 v[42:45], v[70:73], v[78:81], v[42:45]
	s_mov_b32 m0, s69
	s_add_i32 s70, s43, 0x4000
	global_load_lds_dwordx4 v[174:175], off
	s_waitcnt lgkmcnt(5)
	v_mfma_f32_16x16x32_f16 v[30:33], v[66:69], v[86:89], v[30:33]
	ds_read_b128 v[158:161], v180
	v_mfma_f32_16x16x32_f16 v[14:17], v[70:73], v[86:89], v[14:17]
	s_and_b32 s70, s70, 0xc000
	s_add_i32 s71, s69, 0x400
	v_lshl_add_u64 v[176:177], v[174:175], 0, s[26:27]
	s_waitcnt lgkmcnt(5)
	v_mfma_f32_16x16x32_f16 v[26:29], v[66:69], v[82:85], v[26:29]
	ds_read_b128 v[162:165], v180 offset:2048
	v_mfma_f32_16x16x32_f16 v[18:21], v[70:73], v[82:85], v[18:21]
	v_add_u32_e32 v182, s70, v118
	s_add_i32 s72, s74, 204
	s_waitcnt lgkmcnt(5)
	v_mfma_f32_16x16x32_f16 v[54:57], v[94:97], v[74:77], v[54:57]
	s_waitcnt lgkmcnt(4)
	v_mfma_f32_16x16x32_f16 v[50:53], v[90:93], v[74:77], v[50:53]
	v_mfma_f32_16x16x32_f16 v[38:41], v[94:97], v[78:81], v[38:41]
	v_mfma_f32_16x16x32_f16 v[34:37], v[90:93], v[78:81], v[34:37]
	v_add_u32_e32 v178, s72, v116
	v_mfma_f32_16x16x32_f16 v[6:9], v[94:97], v[86:89], v[6:9]
	ds_read_b128 v[166:169], v183 offset:4096
	v_mfma_f32_16x16x32_f16 v[2:5], v[90:93], v[86:89], v[2:5]
	v_lshlrev_b32_e32 v179, 7, v178
	v_bitop3_b32 v178, v178, v112, 6 bitop3:0x6c
	v_mfma_f32_16x16x32_f16 v[22:25], v[94:97], v[82:85], v[22:25]
	ds_read_b128 v[170:173], v183 offset:6144
	v_mfma_f32_16x16x32_f16 v[10:13], v[90:93], v[82:85], v[10:13]
	v_lshl_or_b32 v140, v178, 4, v179
	v_add_u32_e32 v183, s70, v119
	s_waitcnt lgkmcnt(5)
	v_mfma_f32_16x16x32_f16 v[62:65], v[142:145], v[150:153], v[62:65]
	ds_read_b128 v[66:69], v182
	s_waitcnt lgkmcnt(5)
	v_mfma_f32_16x16x32_f16 v[58:61], v[146:149], v[150:153], v[58:61]
	s_mov_b32 m0, s71
	s_addk_i32 s43, 0x4000
	global_load_lds_dwordx4 v[176:177], off
	v_mfma_f32_16x16x32_f16 v[46:49], v[142:145], v[154:157], v[46:49]
	ds_read_b128 v[70:73], v182 offset:2048
	v_mfma_f32_16x16x32_f16 v[42:45], v[146:149], v[154:157], v[42:45]
	s_waitcnt lgkmcnt(5)
	v_mfma_f32_16x16x32_f16 v[30:33], v[142:145], v[158:161], v[30:33]
	ds_read_b128 v[74:77], v140
	v_mfma_f32_16x16x32_f16 v[14:17], v[146:149], v[158:161], v[14:17]
	s_waitcnt lgkmcnt(5)
	v_mfma_f32_16x16x32_f16 v[26:29], v[142:145], v[162:165], v[26:29]
	ds_read_b128 v[78:81], v140 offset:2048
	v_mfma_f32_16x16x32_f16 v[18:21], v[146:149], v[162:165], v[18:21]
	s_waitcnt lgkmcnt(5)
	v_mfma_f32_16x16x32_f16 v[54:57], v[166:169], v[150:153], v[54:57]
	s_waitcnt lgkmcnt(4)
	v_mfma_f32_16x16x32_f16 v[50:53], v[170:173], v[150:153], v[50:53]
	v_mfma_f32_16x16x32_f16 v[38:41], v[166:169], v[154:157], v[38:41]
	v_mfma_f32_16x16x32_f16 v[34:37], v[170:173], v[154:157], v[34:37]
	v_mfma_f32_16x16x32_f16 v[6:9], v[166:169], v[158:161], v[6:9]
	ds_read_b128 v[94:97], v182 offset:4096
	v_mfma_f32_16x16x32_f16 v[2:5], v[170:173], v[158:161], v[2:5]
	v_mfma_f32_16x16x32_f16 v[22:25], v[166:169], v[162:165], v[22:25]
	ds_read_b128 v[90:93], v182 offset:6144
	v_mfma_f32_16x16x32_f16 v[10:13], v[170:173], v[162:165], v[10:13]
	s_waitcnt vmcnt(2)
	s_barrier
	s_waitcnt lgkmcnt(5)
	v_mfma_f32_16x16x32_f16 v[62:65], v[66:69], v[86:89], v[62:65]
	ds_read_b128 v[142:145], v183
	s_waitcnt lgkmcnt(5)
	v_mfma_f32_16x16x32_f16 v[58:61], v[70:73], v[86:89], v[58:61]
	v_xor_b32_e32 v180, 64, v140
	s_add_i32 s67, s62, 22
	s_add_i32 s67, s67, s68
	s_lshl_b32 s64, s67, 13
	v_mfma_f32_16x16x32_f16 v[46:49], v[66:69], v[82:85], v[46:49]
	ds_read_b128 v[146:149], v183 offset:2048
	v_lshl_add_u64 v[174:175], v[100:101], 0, s[64:65]
	s_add_i32 s69, s43, 0xc000
	s_and_b32 s69, s69, 0xc000
	s_add_i32 s69, s69, s42
	v_mfma_f32_16x16x32_f16 v[42:45], v[70:73], v[82:85], v[42:45]
	s_mov_b32 m0, s69
	s_add_i32 s70, s43, 0x4000
	global_load_lds_dwordx4 v[174:175], off
	s_waitcnt lgkmcnt(5)
	v_mfma_f32_16x16x32_f16 v[30:33], v[66:69], v[74:77], v[30:33]
	ds_read_b128 v[150:153], v180
	v_mfma_f32_16x16x32_f16 v[14:17], v[70:73], v[74:77], v[14:17]
	s_and_b32 s70, s70, 0xc000
	s_add_i32 s71, s69, 0x400
	v_lshl_add_u64 v[176:177], v[174:175], 0, s[26:27]
	s_waitcnt lgkmcnt(5)
	v_mfma_f32_16x16x32_f16 v[26:29], v[66:69], v[78:81], v[26:29]
	ds_read_b128 v[154:157], v180 offset:2048
	v_mfma_f32_16x16x32_f16 v[18:21], v[70:73], v[78:81], v[18:21]
	v_add_u32_e32 v182, s70, v118
	s_add_i32 s72, s74, 255
	s_waitcnt lgkmcnt(5)
	v_mfma_f32_16x16x32_f16 v[54:57], v[94:97], v[86:89], v[54:57]
	s_waitcnt lgkmcnt(4)
	v_mfma_f32_16x16x32_f16 v[50:53], v[90:93], v[86:89], v[50:53]
	v_mfma_f32_16x16x32_f16 v[38:41], v[94:97], v[82:85], v[38:41]
	v_mfma_f32_16x16x32_f16 v[34:37], v[90:93], v[82:85], v[34:37]
	v_add_u32_e32 v178, s72, v116
	v_mfma_f32_16x16x32_f16 v[6:9], v[94:97], v[74:77], v[6:9]
	ds_read_b128 v[166:169], v183 offset:4096
	v_mfma_f32_16x16x32_f16 v[2:5], v[90:93], v[74:77], v[2:5]
	v_lshlrev_b32_e32 v179, 7, v178
	v_bitop3_b32 v178, v178, v112, 6 bitop3:0x6c
	v_mfma_f32_16x16x32_f16 v[22:25], v[94:97], v[78:81], v[22:25]
	ds_read_b128 v[170:173], v183 offset:6144
	v_mfma_f32_16x16x32_f16 v[10:13], v[90:93], v[78:81], v[10:13]
	v_lshl_or_b32 v140, v178, 4, v179
	v_add_u32_e32 v183, s70, v119
	s_waitcnt lgkmcnt(5)
	v_mfma_f32_16x16x32_f16 v[62:65], v[142:145], v[158:161], v[62:65]
	ds_read_b128 v[66:69], v182
	s_waitcnt lgkmcnt(5)
	v_mfma_f32_16x16x32_f16 v[58:61], v[146:149], v[158:161], v[58:61]
	s_mov_b32 m0, s71
	s_addk_i32 s43, 0x4000
	global_load_lds_dwordx4 v[176:177], off
	v_mfma_f32_16x16x32_f16 v[46:49], v[142:145], v[162:165], v[46:49]
	ds_read_b128 v[70:73], v182 offset:2048
	v_mfma_f32_16x16x32_f16 v[42:45], v[146:149], v[162:165], v[42:45]
	s_waitcnt lgkmcnt(5)
	v_mfma_f32_16x16x32_f16 v[30:33], v[142:145], v[150:153], v[30:33]
	ds_read_b128 v[86:89], v140
	v_mfma_f32_16x16x32_f16 v[14:17], v[146:149], v[150:153], v[14:17]
	s_waitcnt lgkmcnt(5)
	v_mfma_f32_16x16x32_f16 v[26:29], v[142:145], v[154:157], v[26:29]
	ds_read_b128 v[82:85], v140 offset:2048
	v_mfma_f32_16x16x32_f16 v[18:21], v[146:149], v[154:157], v[18:21]
	s_waitcnt lgkmcnt(5)
	v_mfma_f32_16x16x32_f16 v[54:57], v[166:169], v[158:161], v[54:57]
	s_waitcnt lgkmcnt(4)
	v_mfma_f32_16x16x32_f16 v[50:53], v[170:173], v[158:161], v[50:53]
	v_mfma_f32_16x16x32_f16 v[38:41], v[166:169], v[162:165], v[38:41]
	v_mfma_f32_16x16x32_f16 v[34:37], v[170:173], v[162:165], v[34:37]
	v_mfma_f32_16x16x32_f16 v[6:9], v[166:169], v[150:153], v[6:9]
	ds_read_b128 v[94:97], v182 offset:4096
	v_mfma_f32_16x16x32_f16 v[2:5], v[170:173], v[150:153], v[2:5]
	v_mfma_f32_16x16x32_f16 v[22:25], v[166:169], v[154:157], v[22:25]
	ds_read_b128 v[90:93], v182 offset:6144
	v_mfma_f32_16x16x32_f16 v[10:13], v[170:173], v[154:157], v[10:13]
	s_waitcnt vmcnt(2)
	s_barrier
	s_waitcnt lgkmcnt(5)
	v_mfma_f32_16x16x32_f16 v[62:65], v[66:69], v[74:77], v[62:65]
	ds_read_b128 v[142:145], v183
	s_waitcnt lgkmcnt(5)
	v_mfma_f32_16x16x32_f16 v[58:61], v[70:73], v[74:77], v[58:61]
	v_xor_b32_e32 v180, 64, v140
	s_add_i32 s67, s62, 42
	s_add_i32 s67, s67, s68
	s_lshl_b32 s64, s67, 13
	v_mfma_f32_16x16x32_f16 v[46:49], v[66:69], v[78:81], v[46:49]
	ds_read_b128 v[146:149], v183 offset:2048
	v_lshl_add_u64 v[174:175], v[100:101], 0, s[64:65]
	s_add_i32 s69, s43, 0xc000
	s_and_b32 s69, s69, 0xc000
	s_add_i32 s69, s69, s42
	v_mfma_f32_16x16x32_f16 v[42:45], v[70:73], v[78:81], v[42:45]
	s_mov_b32 m0, s69
	s_add_i32 s70, s43, 0x4000
	global_load_lds_dwordx4 v[174:175], off
	s_waitcnt lgkmcnt(5)
	v_mfma_f32_16x16x32_f16 v[30:33], v[66:69], v[86:89], v[30:33]
	ds_read_b128 v[158:161], v180
	v_mfma_f32_16x16x32_f16 v[14:17], v[70:73], v[86:89], v[14:17]
	s_and_b32 s70, s70, 0xc000
	s_add_i32 s71, s69, 0x400
	v_lshl_add_u64 v[176:177], v[174:175], 0, s[26:27]
	s_waitcnt lgkmcnt(5)
	v_mfma_f32_16x16x32_f16 v[26:29], v[66:69], v[82:85], v[26:29]
	ds_read_b128 v[162:165], v180 offset:2048
	v_mfma_f32_16x16x32_f16 v[18:21], v[70:73], v[82:85], v[18:21]
	v_add_u32_e32 v182, s70, v118
	s_add_i32 s72, s74, 53
	s_waitcnt lgkmcnt(5)
	v_mfma_f32_16x16x32_f16 v[54:57], v[94:97], v[74:77], v[54:57]
	s_waitcnt lgkmcnt(4)
	v_mfma_f32_16x16x32_f16 v[50:53], v[90:93], v[74:77], v[50:53]
	v_mfma_f32_16x16x32_f16 v[38:41], v[94:97], v[78:81], v[38:41]
	v_mfma_f32_16x16x32_f16 v[34:37], v[90:93], v[78:81], v[34:37]
	v_add_u32_e32 v178, s72, v116
	v_mfma_f32_16x16x32_f16 v[6:9], v[94:97], v[86:89], v[6:9]
	ds_read_b128 v[166:169], v183 offset:4096
	v_mfma_f32_16x16x32_f16 v[2:5], v[90:93], v[86:89], v[2:5]
	v_lshlrev_b32_e32 v179, 7, v178
	v_bitop3_b32 v178, v178, v112, 6 bitop3:0x6c
	v_mfma_f32_16x16x32_f16 v[22:25], v[94:97], v[82:85], v[22:25]
	ds_read_b128 v[170:173], v183 offset:6144
	v_mfma_f32_16x16x32_f16 v[10:13], v[90:93], v[82:85], v[10:13]
	v_lshl_or_b32 v140, v178, 4, v179
	v_add_u32_e32 v183, s70, v119
	s_waitcnt lgkmcnt(5)
	v_mfma_f32_16x16x32_f16 v[62:65], v[142:145], v[150:153], v[62:65]
	ds_read_b128 v[66:69], v182
	s_waitcnt lgkmcnt(5)
	v_mfma_f32_16x16x32_f16 v[58:61], v[146:149], v[150:153], v[58:61]
	s_mov_b32 m0, s71
	s_addk_i32 s43, 0x4000
	global_load_lds_dwordx4 v[176:177], off
	v_mfma_f32_16x16x32_f16 v[46:49], v[142:145], v[154:157], v[46:49]
	ds_read_b128 v[70:73], v182 offset:2048
	v_mfma_f32_16x16x32_f16 v[42:45], v[146:149], v[154:157], v[42:45]
	s_sub_i32 s72, s72, 51
	v_add_u32_e32 v178, s72, v116
	s_waitcnt lgkmcnt(5)
	v_mfma_f32_16x16x32_f16 v[30:33], v[142:145], v[158:161], v[30:33]
	ds_read_b128 v[74:77], v140
	v_mfma_f32_16x16x32_f16 v[14:17], v[146:149], v[158:161], v[14:17]
	v_lshlrev_b32_e32 v179, 7, v178
	v_bitop3_b32 v178, v178, v112, 6 bitop3:0x6c
	s_waitcnt lgkmcnt(5)
	v_mfma_f32_16x16x32_f16 v[26:29], v[142:145], v[162:165], v[26:29]
	ds_read_b128 v[78:81], v140 offset:2048
	v_mfma_f32_16x16x32_f16 v[18:21], v[146:149], v[162:165], v[18:21]
	v_lshl_or_b32 v139, v178, 4, v179
	s_waitcnt lgkmcnt(5)
	v_mfma_f32_16x16x32_f16 v[54:57], v[166:169], v[150:153], v[54:57]
	ds_read_b128 v[86:89], v139
	s_waitcnt lgkmcnt(5)
	v_mfma_f32_16x16x32_f16 v[50:53], v[170:173], v[150:153], v[50:53]
	v_mfma_f32_16x16x32_f16 v[38:41], v[166:169], v[154:157], v[38:41]
	ds_read_b128 v[82:85], v139 offset:2048
	v_mfma_f32_16x16x32_f16 v[34:37], v[170:173], v[154:157], v[34:37]
	v_mfma_f32_16x16x32_f16 v[6:9], v[166:169], v[158:161], v[6:9]
	ds_read_b128 v[94:97], v182 offset:4096
	v_mfma_f32_16x16x32_f16 v[2:5], v[170:173], v[158:161], v[2:5]
	v_mfma_f32_16x16x32_f16 v[22:25], v[166:169], v[162:165], v[22:25]
	ds_read_b128 v[90:93], v182 offset:6144
	v_mfma_f32_16x16x32_f16 v[10:13], v[170:173], v[162:165], v[10:13]
	s_waitcnt vmcnt(2)
	s_barrier
	s_waitcnt lgkmcnt(3)
	v_mfma_f32_16x16x32_f16 v[62:65], v[66:69], v[86:89], v[62:65]
	ds_read_b128 v[142:145], v183
	v_mfma_f32_16x16x32_f16 v[58:61], v[70:73], v[86:89], v[58:61]
	v_xor_b32_e32 v180, 64, v140
	s_add_i32 s67, s62, 62
	s_add_i32 s67, s67, s68
	s_lshl_b32 s64, s67, 13
	s_waitcnt lgkmcnt(3)
	v_mfma_f32_16x16x32_f16 v[46:49], v[66:69], v[82:85], v[46:49]
	ds_read_b128 v[146:149], v183 offset:2048
	v_lshl_add_u64 v[174:175], v[100:101], 0, s[64:65]
	s_add_i32 s69, s43, 0xc000
	s_and_b32 s69, s69, 0xc000
	s_add_i32 s69, s69, s42
	v_mfma_f32_16x16x32_f16 v[42:45], v[70:73], v[82:85], v[42:45]
	v_xor_b32_e32 v181, 64, v139
	s_mov_b32 m0, s69
	s_add_i32 s70, s43, 0x4000
	global_load_lds_dwordx4 v[174:175], off
	v_mfma_f32_16x16x32_f16 v[30:33], v[66:69], v[74:77], v[30:33]
	ds_read_b128 v[150:153], v180
	v_mfma_f32_16x16x32_f16 v[14:17], v[70:73], v[74:77], v[14:17]
	s_and_b32 s70, s70, 0xc000
	s_add_i32 s71, s69, 0x400
	v_lshl_add_u64 v[176:177], v[174:175], 0, s[26:27]
	v_mfma_f32_16x16x32_f16 v[26:29], v[66:69], v[78:81], v[26:29]
	ds_read_b128 v[154:157], v180 offset:2048
	v_mfma_f32_16x16x32_f16 v[18:21], v[70:73], v[78:81], v[18:21]
	v_add_u32_e32 v182, s70, v118
	s_add_i32 s72, s74, 104
	s_waitcnt lgkmcnt(5)
	v_mfma_f32_16x16x32_f16 v[54:57], v[94:97], v[86:89], v[54:57]
	ds_read_b128 v[158:161], v181
	s_waitcnt lgkmcnt(5)
	v_mfma_f32_16x16x32_f16 v[50:53], v[90:93], v[86:89], v[50:53]
	v_mfma_f32_16x16x32_f16 v[38:41], v[94:97], v[82:85], v[38:41]
	ds_read_b128 v[162:165], v181 offset:2048
	v_mfma_f32_16x16x32_f16 v[34:37], v[90:93], v[82:85], v[34:37]
	v_add_u32_e32 v178, s72, v116
	v_mfma_f32_16x16x32_f16 v[6:9], v[94:97], v[74:77], v[6:9]
	ds_read_b128 v[166:169], v183 offset:4096
	v_mfma_f32_16x16x32_f16 v[2:5], v[90:93], v[74:77], v[2:5]
	v_lshlrev_b32_e32 v179, 7, v178
	v_bitop3_b32 v178, v178, v112, 6 bitop3:0x6c
	v_mfma_f32_16x16x32_f16 v[22:25], v[94:97], v[78:81], v[22:25]
	ds_read_b128 v[170:173], v183 offset:6144
	v_mfma_f32_16x16x32_f16 v[10:13], v[90:93], v[78:81], v[10:13]
	v_lshl_or_b32 v140, v178, 4, v179
	v_add_u32_e32 v183, s70, v119
	s_waitcnt lgkmcnt(3)
	v_mfma_f32_16x16x32_f16 v[62:65], v[142:145], v[158:161], v[62:65]
	ds_read_b128 v[66:69], v182
	v_mfma_f32_16x16x32_f16 v[58:61], v[146:149], v[158:161], v[58:61]
	s_mov_b32 m0, s71
	s_addk_i32 s43, 0x4000
	global_load_lds_dwordx4 v[176:177], off
	s_waitcnt lgkmcnt(3)
	v_mfma_f32_16x16x32_f16 v[46:49], v[142:145], v[162:165], v[46:49]
	ds_read_b128 v[70:73], v182 offset:2048
	v_mfma_f32_16x16x32_f16 v[42:45], v[146:149], v[162:165], v[42:45]
	v_mfma_f32_16x16x32_f16 v[30:33], v[142:145], v[150:153], v[30:33]
	ds_read_b128 v[86:89], v140
	v_mfma_f32_16x16x32_f16 v[14:17], v[146:149], v[150:153], v[14:17]
	v_mfma_f32_16x16x32_f16 v[26:29], v[142:145], v[154:157], v[26:29]
	ds_read_b128 v[82:85], v140 offset:2048
	v_mfma_f32_16x16x32_f16 v[18:21], v[146:149], v[154:157], v[18:21]
	s_waitcnt lgkmcnt(5)
	v_mfma_f32_16x16x32_f16 v[54:57], v[166:169], v[158:161], v[54:57]
	s_waitcnt lgkmcnt(4)
	v_mfma_f32_16x16x32_f16 v[50:53], v[170:173], v[158:161], v[50:53]
	v_mfma_f32_16x16x32_f16 v[38:41], v[166:169], v[162:165], v[38:41]
	v_mfma_f32_16x16x32_f16 v[34:37], v[170:173], v[162:165], v[34:37]
	v_mfma_f32_16x16x32_f16 v[6:9], v[166:169], v[150:153], v[6:9]
	ds_read_b128 v[94:97], v182 offset:4096
	v_mfma_f32_16x16x32_f16 v[2:5], v[170:173], v[150:153], v[2:5]
	v_mfma_f32_16x16x32_f16 v[22:25], v[166:169], v[154:157], v[22:25]
	ds_read_b128 v[90:93], v182 offset:6144
	v_mfma_f32_16x16x32_f16 v[10:13], v[170:173], v[154:157], v[10:13]
	s_waitcnt vmcnt(2)
	s_barrier
	s_waitcnt lgkmcnt(5)
	v_mfma_f32_16x16x32_f16 v[62:65], v[66:69], v[74:77], v[62:65]
	ds_read_b128 v[142:145], v183
	s_waitcnt lgkmcnt(5)
	v_mfma_f32_16x16x32_f16 v[58:61], v[70:73], v[74:77], v[58:61]
	v_xor_b32_e32 v180, 64, v140
	s_add_i32 s67, s62, 82
	s_add_i32 s67, s67, s68
	s_lshl_b32 s64, s67, 13
	v_mfma_f32_16x16x32_f16 v[46:49], v[66:69], v[78:81], v[46:49]
	ds_read_b128 v[146:149], v183 offset:2048
	v_lshl_add_u64 v[174:175], v[100:101], 0, s[64:65]
	s_add_i32 s69, s43, 0xc000
	s_and_b32 s69, s69, 0xc000
	s_add_i32 s69, s69, s42
	v_mfma_f32_16x16x32_f16 v[42:45], v[70:73], v[78:81], v[42:45]
	s_mov_b32 m0, s69
	s_add_i32 s70, s43, 0x4000
	global_load_lds_dwordx4 v[174:175], off
	s_waitcnt lgkmcnt(5)
	v_mfma_f32_16x16x32_f16 v[30:33], v[66:69], v[86:89], v[30:33]
	ds_read_b128 v[158:161], v180
	v_mfma_f32_16x16x32_f16 v[14:17], v[70:73], v[86:89], v[14:17]
	s_and_b32 s70, s70, 0xc000
	s_add_i32 s71, s69, 0x400
	v_lshl_add_u64 v[176:177], v[174:175], 0, s[26:27]
	s_waitcnt lgkmcnt(5)
	v_mfma_f32_16x16x32_f16 v[26:29], v[66:69], v[82:85], v[26:29]
	ds_read_b128 v[162:165], v180 offset:2048
	v_mfma_f32_16x16x32_f16 v[18:21], v[70:73], v[82:85], v[18:21]
	v_add_u32_e32 v182, s70, v118
	s_add_i32 s72, s74, 155
	s_waitcnt lgkmcnt(5)
	v_mfma_f32_16x16x32_f16 v[54:57], v[94:97], v[74:77], v[54:57]
	s_waitcnt lgkmcnt(4)
	v_mfma_f32_16x16x32_f16 v[50:53], v[90:93], v[74:77], v[50:53]
	v_mfma_f32_16x16x32_f16 v[38:41], v[94:97], v[78:81], v[38:41]
	v_mfma_f32_16x16x32_f16 v[34:37], v[90:93], v[78:81], v[34:37]
	v_add_u32_e32 v178, s72, v116
	v_mfma_f32_16x16x32_f16 v[6:9], v[94:97], v[86:89], v[6:9]
	ds_read_b128 v[166:169], v183 offset:4096
	v_mfma_f32_16x16x32_f16 v[2:5], v[90:93], v[86:89], v[2:5]
	v_lshlrev_b32_e32 v179, 7, v178
	v_bitop3_b32 v178, v178, v112, 6 bitop3:0x6c
	v_mfma_f32_16x16x32_f16 v[22:25], v[94:97], v[82:85], v[22:25]
	ds_read_b128 v[170:173], v183 offset:6144
	v_mfma_f32_16x16x32_f16 v[10:13], v[90:93], v[82:85], v[10:13]
	v_lshl_or_b32 v140, v178, 4, v179
	v_add_u32_e32 v183, s70, v119
	s_waitcnt lgkmcnt(5)
	v_mfma_f32_16x16x32_f16 v[62:65], v[142:145], v[150:153], v[62:65]
	ds_read_b128 v[66:69], v182
	s_waitcnt lgkmcnt(5)
	v_mfma_f32_16x16x32_f16 v[58:61], v[146:149], v[150:153], v[58:61]
	s_mov_b32 m0, s71
	s_addk_i32 s43, 0x4000
	global_load_lds_dwordx4 v[176:177], off
	v_mfma_f32_16x16x32_f16 v[46:49], v[142:145], v[154:157], v[46:49]
	ds_read_b128 v[70:73], v182 offset:2048
	v_mfma_f32_16x16x32_f16 v[42:45], v[146:149], v[154:157], v[42:45]
	s_waitcnt lgkmcnt(5)
	v_mfma_f32_16x16x32_f16 v[30:33], v[142:145], v[158:161], v[30:33]
	ds_read_b128 v[74:77], v140
	v_mfma_f32_16x16x32_f16 v[14:17], v[146:149], v[158:161], v[14:17]
	s_waitcnt lgkmcnt(5)
	v_mfma_f32_16x16x32_f16 v[26:29], v[142:145], v[162:165], v[26:29]
	ds_read_b128 v[78:81], v140 offset:2048
	v_mfma_f32_16x16x32_f16 v[18:21], v[146:149], v[162:165], v[18:21]
	s_waitcnt lgkmcnt(5)
	v_mfma_f32_16x16x32_f16 v[54:57], v[166:169], v[150:153], v[54:57]
	s_waitcnt lgkmcnt(4)
	v_mfma_f32_16x16x32_f16 v[50:53], v[170:173], v[150:153], v[50:53]
	v_mfma_f32_16x16x32_f16 v[38:41], v[166:169], v[154:157], v[38:41]
	v_mfma_f32_16x16x32_f16 v[34:37], v[170:173], v[154:157], v[34:37]
	v_mfma_f32_16x16x32_f16 v[6:9], v[166:169], v[158:161], v[6:9]
	ds_read_b128 v[94:97], v182 offset:4096
	v_mfma_f32_16x16x32_f16 v[2:5], v[170:173], v[158:161], v[2:5]
	v_mfma_f32_16x16x32_f16 v[22:25], v[166:169], v[162:165], v[22:25]
	ds_read_b128 v[90:93], v182 offset:6144
	v_mfma_f32_16x16x32_f16 v[10:13], v[170:173], v[162:165], v[10:13]
	s_waitcnt vmcnt(2)
	s_barrier
	s_waitcnt lgkmcnt(5)
	v_mfma_f32_16x16x32_f16 v[62:65], v[66:69], v[86:89], v[62:65]
	ds_read_b128 v[142:145], v183
	s_waitcnt lgkmcnt(5)
	v_mfma_f32_16x16x32_f16 v[58:61], v[70:73], v[86:89], v[58:61]
	v_xor_b32_e32 v180, 64, v140
	s_add_i32 s67, s62, 4
	s_add_i32 s67, s67, s68
	s_add_i32 s67, s67, s66
	s_lshl_b32 s64, s67, 13
	v_mfma_f32_16x16x32_f16 v[46:49], v[66:69], v[82:85], v[46:49]
	ds_read_b128 v[146:149], v183 offset:2048
	v_lshl_add_u64 v[174:175], v[100:101], 0, s[64:65]
	s_add_i32 s69, s43, 0xc000
	s_and_b32 s69, s69, 0xc000
	s_add_i32 s69, s69, s42
	v_mfma_f32_16x16x32_f16 v[42:45], v[70:73], v[82:85], v[42:45]
	s_mov_b32 m0, s69
	s_add_i32 s70, s43, 0x4000
	global_load_lds_dwordx4 v[174:175], off
	s_waitcnt lgkmcnt(5)
	v_mfma_f32_16x16x32_f16 v[30:33], v[66:69], v[74:77], v[30:33]
	ds_read_b128 v[150:153], v180
	v_mfma_f32_16x16x32_f16 v[14:17], v[70:73], v[74:77], v[14:17]
	s_and_b32 s70, s70, 0xc000
	s_add_i32 s71, s69, 0x400
	v_lshl_add_u64 v[176:177], v[174:175], 0, s[26:27]
	s_waitcnt lgkmcnt(5)
	v_mfma_f32_16x16x32_f16 v[26:29], v[66:69], v[78:81], v[26:29]
	ds_read_b128 v[154:157], v180 offset:2048
	v_mfma_f32_16x16x32_f16 v[18:21], v[70:73], v[78:81], v[18:21]
	v_add_u32_e32 v182, s70, v118
	s_add_i32 s72, s74, 206
	s_waitcnt lgkmcnt(5)
	v_mfma_f32_16x16x32_f16 v[54:57], v[94:97], v[86:89], v[54:57]
	s_waitcnt lgkmcnt(4)
	v_mfma_f32_16x16x32_f16 v[50:53], v[90:93], v[86:89], v[50:53]
	v_mfma_f32_16x16x32_f16 v[38:41], v[94:97], v[82:85], v[38:41]
	v_mfma_f32_16x16x32_f16 v[34:37], v[90:93], v[82:85], v[34:37]
	v_add_u32_e32 v178, s72, v116
	v_mfma_f32_16x16x32_f16 v[6:9], v[94:97], v[74:77], v[6:9]
	ds_read_b128 v[166:169], v183 offset:4096
	v_mfma_f32_16x16x32_f16 v[2:5], v[90:93], v[74:77], v[2:5]
	v_lshlrev_b32_e32 v179, 7, v178
	v_bitop3_b32 v178, v178, v112, 6 bitop3:0x6c
	v_mfma_f32_16x16x32_f16 v[22:25], v[94:97], v[78:81], v[22:25]
	ds_read_b128 v[170:173], v183 offset:6144
	v_mfma_f32_16x16x32_f16 v[10:13], v[90:93], v[78:81], v[10:13]
	v_lshl_or_b32 v140, v178, 4, v179
	v_add_u32_e32 v183, s70, v119
	s_waitcnt lgkmcnt(5)
	v_mfma_f32_16x16x32_f16 v[62:65], v[142:145], v[158:161], v[62:65]
	ds_read_b128 v[66:69], v182
	s_waitcnt lgkmcnt(5)
	v_mfma_f32_16x16x32_f16 v[58:61], v[146:149], v[158:161], v[58:61]
	s_mov_b32 m0, s71
	s_addk_i32 s43, 0x4000
	global_load_lds_dwordx4 v[176:177], off
	v_mfma_f32_16x16x32_f16 v[46:49], v[142:145], v[162:165], v[46:49]
	ds_read_b128 v[70:73], v182 offset:2048
	v_mfma_f32_16x16x32_f16 v[42:45], v[146:149], v[162:165], v[42:45]
	s_waitcnt lgkmcnt(5)
	v_mfma_f32_16x16x32_f16 v[30:33], v[142:145], v[150:153], v[30:33]
	ds_read_b128 v[86:89], v140
	v_mfma_f32_16x16x32_f16 v[14:17], v[146:149], v[150:153], v[14:17]
	s_waitcnt lgkmcnt(5)
	v_mfma_f32_16x16x32_f16 v[26:29], v[142:145], v[154:157], v[26:29]
	ds_read_b128 v[82:85], v140 offset:2048
	v_mfma_f32_16x16x32_f16 v[18:21], v[146:149], v[154:157], v[18:21]
	s_waitcnt lgkmcnt(5)
	v_mfma_f32_16x16x32_f16 v[54:57], v[166:169], v[158:161], v[54:57]
	s_waitcnt lgkmcnt(4)
	v_mfma_f32_16x16x32_f16 v[50:53], v[170:173], v[158:161], v[50:53]
	v_mfma_f32_16x16x32_f16 v[38:41], v[166:169], v[162:165], v[38:41]
	v_mfma_f32_16x16x32_f16 v[34:37], v[170:173], v[162:165], v[34:37]
	v_mfma_f32_16x16x32_f16 v[6:9], v[166:169], v[150:153], v[6:9]
	ds_read_b128 v[94:97], v182 offset:4096
	v_mfma_f32_16x16x32_f16 v[2:5], v[170:173], v[150:153], v[2:5]
	v_mfma_f32_16x16x32_f16 v[22:25], v[166:169], v[154:157], v[22:25]
	ds_read_b128 v[90:93], v182 offset:6144
	v_mfma_f32_16x16x32_f16 v[10:13], v[170:173], v[154:157], v[10:13]
	s_waitcnt vmcnt(2)
	s_barrier
	s_waitcnt lgkmcnt(5)
	v_mfma_f32_16x16x32_f16 v[62:65], v[66:69], v[74:77], v[62:65]
	ds_read_b128 v[142:145], v183
	s_waitcnt lgkmcnt(5)
	v_mfma_f32_16x16x32_f16 v[58:61], v[70:73], v[74:77], v[58:61]
	v_xor_b32_e32 v180, 64, v140
	s_add_i32 s67, s62, 24
	s_add_i32 s67, s67, s68
	s_add_i32 s67, s67, s66
	s_lshl_b32 s64, s67, 13
	v_mfma_f32_16x16x32_f16 v[46:49], v[66:69], v[78:81], v[46:49]
	ds_read_b128 v[146:149], v183 offset:2048
	v_lshl_add_u64 v[174:175], v[100:101], 0, s[64:65]
	s_add_i32 s69, s43, 0xc000
	s_and_b32 s69, s69, 0xc000
	s_add_i32 s69, s69, s42
	v_mfma_f32_16x16x32_f16 v[42:45], v[70:73], v[78:81], v[42:45]
	s_mov_b32 m0, s69
	s_add_i32 s70, s43, 0x4000
	global_load_lds_dwordx4 v[174:175], off
	s_waitcnt lgkmcnt(5)
	v_mfma_f32_16x16x32_f16 v[30:33], v[66:69], v[86:89], v[30:33]
	ds_read_b128 v[158:161], v180
	v_mfma_f32_16x16x32_f16 v[14:17], v[70:73], v[86:89], v[14:17]
	s_and_b32 s70, s70, 0xc000
	s_add_i32 s71, s69, 0x400
	v_lshl_add_u64 v[176:177], v[174:175], 0, s[26:27]
	s_waitcnt lgkmcnt(5)
	v_mfma_f32_16x16x32_f16 v[26:29], v[66:69], v[82:85], v[26:29]
	ds_read_b128 v[162:165], v180 offset:2048
	v_mfma_f32_16x16x32_f16 v[18:21], v[70:73], v[82:85], v[18:21]
	v_add_u32_e32 v182, s70, v118
	s_add_i32 s72, s74, 257
	s_waitcnt lgkmcnt(5)
	v_mfma_f32_16x16x32_f16 v[54:57], v[94:97], v[74:77], v[54:57]
	s_waitcnt lgkmcnt(4)
	v_mfma_f32_16x16x32_f16 v[50:53], v[90:93], v[74:77], v[50:53]
	v_mfma_f32_16x16x32_f16 v[38:41], v[94:97], v[78:81], v[38:41]
	v_mfma_f32_16x16x32_f16 v[34:37], v[90:93], v[78:81], v[34:37]
	v_add_u32_e32 v178, s72, v116
	v_mfma_f32_16x16x32_f16 v[6:9], v[94:97], v[86:89], v[6:9]
	ds_read_b128 v[166:169], v183 offset:4096
	v_mfma_f32_16x16x32_f16 v[2:5], v[90:93], v[86:89], v[2:5]
	v_lshlrev_b32_e32 v179, 7, v178
	v_bitop3_b32 v178, v178, v112, 6 bitop3:0x6c
	v_mfma_f32_16x16x32_f16 v[22:25], v[94:97], v[82:85], v[22:25]
	ds_read_b128 v[170:173], v183 offset:6144
	v_mfma_f32_16x16x32_f16 v[10:13], v[90:93], v[82:85], v[10:13]
	v_lshl_or_b32 v140, v178, 4, v179
	v_add_u32_e32 v183, s70, v119
	s_waitcnt lgkmcnt(5)
	v_mfma_f32_16x16x32_f16 v[62:65], v[142:145], v[150:153], v[62:65]
	ds_read_b128 v[66:69], v182
	s_waitcnt lgkmcnt(5)
	v_mfma_f32_16x16x32_f16 v[58:61], v[146:149], v[150:153], v[58:61]
	s_mov_b32 m0, s71
	s_addk_i32 s43, 0x4000
	global_load_lds_dwordx4 v[176:177], off
	v_mfma_f32_16x16x32_f16 v[46:49], v[142:145], v[154:157], v[46:49]
	ds_read_b128 v[70:73], v182 offset:2048
	v_mfma_f32_16x16x32_f16 v[42:45], v[146:149], v[154:157], v[42:45]
	s_waitcnt lgkmcnt(5)
	v_mfma_f32_16x16x32_f16 v[30:33], v[142:145], v[158:161], v[30:33]
	ds_read_b128 v[74:77], v140
	v_mfma_f32_16x16x32_f16 v[14:17], v[146:149], v[158:161], v[14:17]
	s_waitcnt lgkmcnt(5)
	v_mfma_f32_16x16x32_f16 v[26:29], v[142:145], v[162:165], v[26:29]
	ds_read_b128 v[78:81], v140 offset:2048
	v_mfma_f32_16x16x32_f16 v[18:21], v[146:149], v[162:165], v[18:21]
	s_waitcnt lgkmcnt(5)
	v_mfma_f32_16x16x32_f16 v[54:57], v[166:169], v[150:153], v[54:57]
	s_waitcnt lgkmcnt(4)
	v_mfma_f32_16x16x32_f16 v[50:53], v[170:173], v[150:153], v[50:53]
	v_mfma_f32_16x16x32_f16 v[38:41], v[166:169], v[154:157], v[38:41]
	v_mfma_f32_16x16x32_f16 v[34:37], v[170:173], v[154:157], v[34:37]
	v_mfma_f32_16x16x32_f16 v[6:9], v[166:169], v[158:161], v[6:9]
	ds_read_b128 v[94:97], v182 offset:4096
	v_mfma_f32_16x16x32_f16 v[2:5], v[170:173], v[158:161], v[2:5]
	v_mfma_f32_16x16x32_f16 v[22:25], v[166:169], v[162:165], v[22:25]
	ds_read_b128 v[90:93], v182 offset:6144
	v_mfma_f32_16x16x32_f16 v[10:13], v[170:173], v[162:165], v[10:13]
	s_waitcnt vmcnt(2)
	s_barrier
	s_waitcnt lgkmcnt(5)
	v_mfma_f32_16x16x32_f16 v[62:65], v[66:69], v[86:89], v[62:65]
	ds_read_b128 v[142:145], v183
	s_waitcnt lgkmcnt(5)
	v_mfma_f32_16x16x32_f16 v[58:61], v[70:73], v[86:89], v[58:61]
	v_xor_b32_e32 v180, 64, v140
	s_add_i32 s67, s62, 44
	s_add_i32 s67, s67, s68
	s_add_i32 s67, s67, s66
	s_lshl_b32 s64, s67, 13
	v_mfma_f32_16x16x32_f16 v[46:49], v[66:69], v[82:85], v[46:49]
	ds_read_b128 v[146:149], v183 offset:2048
	v_lshl_add_u64 v[174:175], v[100:101], 0, s[64:65]
	s_add_i32 s69, s43, 0xc000
	s_and_b32 s69, s69, 0xc000
	s_add_i32 s69, s69, s42
	v_mfma_f32_16x16x32_f16 v[42:45], v[70:73], v[82:85], v[42:45]
	s_mov_b32 m0, s69
	s_add_i32 s70, s43, 0x4000
	global_load_lds_dwordx4 v[174:175], off
	s_waitcnt lgkmcnt(5)
	v_mfma_f32_16x16x32_f16 v[30:33], v[66:69], v[74:77], v[30:33]
	ds_read_b128 v[150:153], v180
	v_mfma_f32_16x16x32_f16 v[14:17], v[70:73], v[74:77], v[14:17]
	s_and_b32 s70, s70, 0xc000
	s_add_i32 s71, s69, 0x400
	v_lshl_add_u64 v[176:177], v[174:175], 0, s[26:27]
	s_waitcnt lgkmcnt(5)
	v_mfma_f32_16x16x32_f16 v[26:29], v[66:69], v[78:81], v[26:29]
	ds_read_b128 v[154:157], v180 offset:2048
	v_mfma_f32_16x16x32_f16 v[18:21], v[70:73], v[78:81], v[18:21]
	v_add_u32_e32 v182, s70, v118
	s_add_i32 s72, s74, 55
	s_waitcnt lgkmcnt(5)
	v_mfma_f32_16x16x32_f16 v[54:57], v[94:97], v[86:89], v[54:57]
	s_waitcnt lgkmcnt(4)
	v_mfma_f32_16x16x32_f16 v[50:53], v[90:93], v[86:89], v[50:53]
	v_mfma_f32_16x16x32_f16 v[38:41], v[94:97], v[82:85], v[38:41]
	v_mfma_f32_16x16x32_f16 v[34:37], v[90:93], v[82:85], v[34:37]
	v_add_u32_e32 v178, s72, v116
	v_mfma_f32_16x16x32_f16 v[6:9], v[94:97], v[74:77], v[6:9]
	ds_read_b128 v[166:169], v183 offset:4096
	v_mfma_f32_16x16x32_f16 v[2:5], v[90:93], v[74:77], v[2:5]
	v_lshlrev_b32_e32 v179, 7, v178
	v_bitop3_b32 v178, v178, v112, 6 bitop3:0x6c
	v_mfma_f32_16x16x32_f16 v[22:25], v[94:97], v[78:81], v[22:25]
	ds_read_b128 v[170:173], v183 offset:6144
	v_mfma_f32_16x16x32_f16 v[10:13], v[90:93], v[78:81], v[10:13]
	v_lshl_or_b32 v140, v178, 4, v179
	v_add_u32_e32 v183, s70, v119
	s_waitcnt lgkmcnt(5)
	v_mfma_f32_16x16x32_f16 v[62:65], v[142:145], v[158:161], v[62:65]
	ds_read_b128 v[66:69], v182
	s_waitcnt lgkmcnt(5)
	v_mfma_f32_16x16x32_f16 v[58:61], v[146:149], v[158:161], v[58:61]
	s_mov_b32 m0, s71
	s_addk_i32 s43, 0x4000
	global_load_lds_dwordx4 v[176:177], off
	v_mfma_f32_16x16x32_f16 v[46:49], v[142:145], v[162:165], v[46:49]
	ds_read_b128 v[70:73], v182 offset:2048
	v_mfma_f32_16x16x32_f16 v[42:45], v[146:149], v[162:165], v[42:45]
	s_sub_i32 s72, s72, 51
	v_add_u32_e32 v178, s72, v116
	s_waitcnt lgkmcnt(5)
	v_mfma_f32_16x16x32_f16 v[30:33], v[142:145], v[150:153], v[30:33]
	ds_read_b128 v[86:89], v140
	v_mfma_f32_16x16x32_f16 v[14:17], v[146:149], v[150:153], v[14:17]
	v_lshlrev_b32_e32 v179, 7, v178
	v_bitop3_b32 v178, v178, v112, 6 bitop3:0x6c
	s_waitcnt lgkmcnt(5)
	v_mfma_f32_16x16x32_f16 v[26:29], v[142:145], v[154:157], v[26:29]
	ds_read_b128 v[82:85], v140 offset:2048
	v_mfma_f32_16x16x32_f16 v[18:21], v[146:149], v[154:157], v[18:21]
	v_lshl_or_b32 v139, v178, 4, v179
	s_waitcnt lgkmcnt(5)
	v_mfma_f32_16x16x32_f16 v[54:57], v[166:169], v[158:161], v[54:57]
	ds_read_b128 v[74:77], v139
	s_waitcnt lgkmcnt(5)
	v_mfma_f32_16x16x32_f16 v[50:53], v[170:173], v[158:161], v[50:53]
	v_mfma_f32_16x16x32_f16 v[38:41], v[166:169], v[162:165], v[38:41]
	ds_read_b128 v[78:81], v139 offset:2048
	v_mfma_f32_16x16x32_f16 v[34:37], v[170:173], v[162:165], v[34:37]
	s_add_i32 s62, s62, 4
	s_add_i32 s74, s74, 4
	s_add_i32 s60, s60, 1
	v_mfma_f32_16x16x32_f16 v[6:9], v[166:169], v[150:153], v[6:9]
	ds_read_b128 v[94:97], v182 offset:4096
	v_mfma_f32_16x16x32_f16 v[2:5], v[170:173], v[150:153], v[2:5]
	s_cmp_eq_u32 s60, 4
	s_cselect_b32 s66, 0x17c, 0
	v_mfma_f32_16x16x32_f16 v[22:25], v[166:169], v[154:157], v[22:25]
	ds_read_b128 v[90:93], v182 offset:6144
	s_cmp_eq_u32 s60, s61
	v_mfma_f32_16x16x32_f16 v[10:13], v[170:173], v[154:157], v[10:13]
	s_cbranch_scc0 .Lc6_loop
	s_cmp_eq_u32 s61, 10
	s_cbranch_scc1 .LBB10_49
	s_waitcnt lgkmcnt(0)
	s_mov_b32 s46, 64
	v_mov_b64_e32 v[66:67], s[4:5]
	s_barrier
	s_and_saveexec_b64 s[28:29], s[6:7]
	v_or_b32_e32 v66, s46, v103
	v_lshl_or_b32 v66, v66, 6, v120
	v_ashrrev_i32_e32 v67, 31, v66
	v_lshlrev_b64 v[66:67], 7, v[66:67]
	v_lshl_add_u64 v[66:67], v[98:99], 0, v[66:67]
	s_or_b64 exec, exec, s[28:29]
	v_readfirstlane_b32 s28, v131
	s_mov_b32 m0, s28
	s_nop 0
	global_load_lds_dwordx4 v[66:67], off
	v_mov_b64_e32 v[66:67], s[4:5]
	s_and_saveexec_b64 s[28:29], s[8:9]
	v_or_b32_e32 v66, s46, v105
	v_lshl_or_b32 v66, v66, 6, v121
	v_ashrrev_i32_e32 v67, 31, v66
	v_lshlrev_b64 v[66:67], 7, v[66:67]
	v_lshl_add_u64 v[66:67], v[98:99], 0, v[66:67]
	s_or_b64 exec, exec, s[28:29]
	v_readfirstlane_b32 s28, v132
	s_mov_b32 m0, s28
	s_nop 0
	global_load_lds_dwordx4 v[66:67], off
	v_mov_b64_e32 v[66:67], s[4:5]
	s_and_saveexec_b64 s[28:29], s[10:11]
	v_or_b32_e32 v66, s46, v106
	v_lshl_or_b32 v66, v66, 6, v122
	v_ashrrev_i32_e32 v67, 31, v66
	v_lshlrev_b64 v[66:67], 7, v[66:67]
	v_lshl_add_u64 v[66:67], v[98:99], 0, v[66:67]
	s_or_b64 exec, exec, s[28:29]
	v_readfirstlane_b32 s28, v133
	s_mov_b32 m0, s28
	s_nop 0
	global_load_lds_dwordx4 v[66:67], off
	v_mov_b64_e32 v[66:67], s[4:5]
	s_and_saveexec_b64 s[28:29], s[12:13]
	v_or_b32_e32 v66, s46, v107
	v_lshl_or_b32 v66, v66, 6, v123
	v_ashrrev_i32_e32 v67, 31, v66
	v_lshlrev_b64 v[66:67], 7, v[66:67]
	v_lshl_add_u64 v[66:67], v[98:99], 0, v[66:67]
	s_or_b64 exec, exec, s[28:29]
	v_readfirstlane_b32 s28, v134
	s_mov_b32 m0, s28
	s_nop 0
	global_load_lds_dwordx4 v[66:67], off
	v_mov_b64_e32 v[66:67], s[4:5]
	s_and_saveexec_b64 s[28:29], s[14:15]
	v_or_b32_e32 v66, s46, v108
	v_lshl_or_b32 v66, v66, 6, v124
	v_ashrrev_i32_e32 v67, 31, v66
	v_lshlrev_b64 v[66:67], 7, v[66:67]
	v_lshl_add_u64 v[66:67], v[98:99], 0, v[66:67]
	s_or_b64 exec, exec, s[28:29]
	v_readfirstlane_b32 s28, v135
	s_mov_b32 m0, s28
	s_nop 0
	global_load_lds_dwordx4 v[66:67], off
	v_mov_b64_e32 v[66:67], s[4:5]
	s_and_saveexec_b64 s[28:29], s[16:17]
	v_or_b32_e32 v66, s46, v109
	v_lshl_or_b32 v66, v66, 6, v125
	v_ashrrev_i32_e32 v67, 31, v66
	v_lshlrev_b64 v[66:67], 7, v[66:67]
	v_lshl_add_u64 v[66:67], v[98:99], 0, v[66:67]
	s_or_b64 exec, exec, s[28:29]
	v_readfirstlane_b32 s28, v136
	s_mov_b32 m0, s28
	s_nop 0
	global_load_lds_dwordx4 v[66:67], off
	v_mov_b64_e32 v[66:67], s[4:5]
	s_and_saveexec_b64 s[28:29], s[18:19]
	v_or_b32_e32 v66, s46, v110
	v_lshl_or_b32 v66, v66, 6, v126
	v_ashrrev_i32_e32 v67, 31, v66
	v_lshlrev_b64 v[66:67], 7, v[66:67]
	v_lshl_add_u64 v[66:67], v[98:99], 0, v[66:67]
	s_or_b64 exec, exec, s[28:29]
	v_readfirstlane_b32 s28, v137
	s_mov_b32 m0, s28
	s_nop 0
	global_load_lds_dwordx4 v[66:67], off
	v_mov_b64_e32 v[66:67], s[4:5]
	s_and_saveexec_b64 s[28:29], s[20:21]
	v_or_b32_e32 v66, s46, v113
	v_lshl_or_b32 v66, v66, 6, v127
	v_ashrrev_i32_e32 v67, 31, v66
	v_lshlrev_b64 v[66:67], 7, v[66:67]
	v_lshl_add_u64 v[66:67], v[98:99], 0, v[66:67]
	s_or_b64 exec, exec, s[28:29]
	v_readfirstlane_b32 s28, v138
	s_mov_b32 m0, s28
	s_nop 0
	global_load_lds_dwordx4 v[66:67], off
	v_mov_b64_e32 v[66:67], s[4:5]
	s_and_saveexec_b64 s[28:29], s[22:23]
	v_or_b32_e32 v66, s46, v114
	v_lshl_or_b32 v66, v66, 6, v128
	v_ashrrev_i32_e32 v67, 31, v66
	v_lshlrev_b64 v[66:67], 7, v[66:67]
	v_lshl_add_u64 v[66:67], v[98:99], 0, v[66:67]
	s_or_b64 exec, exec, s[28:29]
	v_add_u32_e32 v68, s38, v104
	s_nop 0
	v_readfirstlane_b32 s28, v68
	s_mov_b32 m0, s28
	s_nop 0
	global_load_lds_dwordx4 v[66:67], off
	v_mov_b64_e32 v[66:67], s[4:5]
	s_and_saveexec_b64 s[28:29], s[24:25]
	s_cbranch_execz .Lc6_seam_tail
	v_or_b32_e32 v66, s46, v115
	v_lshl_or_b32 v66, v66, 6, v129
	v_ashrrev_i32_e32 v67, 31, v66
	v_lshlrev_b64 v[66:67], 7, v[66:67]
	v_lshl_add_u64 v[66:67], v[98:99], 0, v[66:67]
	s_branch .Lc6_seam_tail
.Lc6_seam_tail:
	s_or_b64 exec, exec, s[28:29]
	v_add_u32_e32 v68, s41, v104
	s_nop 0
	v_readfirstlane_b32 s28, v68
	s_mov_b32 m0, s28
	s_and_b32 s28, s43, 0xc000
	global_load_lds_dwordx4 v[66:67], off
	v_add_u32_e32 v178, s40, v116
	v_lshlrev_b32_e32 v179, 7, v178
	v_bitop3_b32 v180, v178, v112, 6 bitop3:0x6c
	v_lshl_or_b32 v139, v180, 4, v179
	v_add_u32_e32 v178, 51, v178
	v_lshlrev_b32_e32 v179, 7, v178
	v_bitop3_b32 v180, v178, v112, 6 bitop3:0x6c
	v_lshl_or_b32 v140, v180, 4, v179
	v_add_u32_e32 v182, s28, v118
	v_add_u32_e32 v183, s28, v119
	s_waitcnt vmcnt(0)
	s_barrier
	ds_read_b128 v[66:69], v182
	ds_read_b128 v[70:73], v182 offset:2048
	ds_read_b128 v[74:77], v139
	ds_read_b128 v[78:81], v139 offset:2048
	ds_read_b128 v[86:89], v140
	ds_read_b128 v[82:85], v140 offset:2048
	ds_read_b128 v[94:97], v182 offset:4096
	ds_read_b128 v[90:93], v182 offset:6144
	s_mov_b32 s62, 0
	s_mov_b32 s74, s40
	s_add_i32 s68, s73, 0x190
	s_mov_b32 s66, 0
	s_mov_b32 s61, 10
	s_waitcnt lgkmcnt(0)
	s_branch .Lc6_loop
